# speedup vs baseline: 1.0300x; 1.0095x over previous
_Z6k_gemmI4Epi8ILi0ELb1ELb1EEEv4GemmT_iiii:
	s_load_dwordx4 s[4:7], s[0:1], 0x38
	s_waitcnt lgkmcnt(0)
	s_mul_i32 s3, s5, s4
	s_mul_i32 s20, s3, s6
	s_cmp_ge_i32 s2, s20
	v_readfirstlane_b32 s3, v0
	s_cbranch_scc1 .LBB4_20
	s_ashr_i32 s21, s20, 31
	s_load_dword s34, s[0:1], 0x10
	s_load_dwordx4 s[16:19], s[0:1], 0x0
	s_load_dwordx8 s[8:15], s[0:1], 0x18
	s_load_dword s33, s[0:1], 0x48
	s_lshr_b32 s0, s21, 29
	v_lshrrev_b32_e32 v5, 5, v0
	s_add_i32 s0, s20, s0
	v_lshlrev_b32_e32 v3, 4, v0
	v_and_b32_e32 v5, 4, v5
	v_lshrrev_b32_e32 v6, 3, v0
	v_lshrrev_b32_e32 v7, 2, v0
	v_lshrrev_b32_e32 v18, 1, v0
	v_lshlrev_b32_e32 v9, 1, v0
	s_ashr_i32 s0, s0, 3
	v_and_b32_e32 v2, 16, v0
	v_and_b32_e32 v4, 0x70, v3
	v_and_b32_e32 v7, 64, v7
	v_and_or_b32 v5, v6, 3, v5
	v_and_b32_e32 v8, 48, v18
	v_and_b32_e32 v9, 64, v9
	s_ff1_i32_b32 s50, s0
	s_lshl_b32 s0, s6, 3
	v_or3_b32 v7, v8, v7, v5
	v_bitop3_b32 v2, v9, v4, v2 bitop3:0x36
	s_ff1_i32_b32 s51, s0
	s_waitcnt lgkmcnt(0)
	v_mad_u64_u32 v[146:147], s[0:1], s34, v6, v[2:3]
	v_mad_u64_u32 v[148:149], s[0:1], s34, v7, v[2:3]
	v_or_b32_e32 v3, 0x2000, v3
	v_lshrrev_b32_e32 v4, 7, v3
	v_lshrrev_b32_e32 v3, 6, v3
	v_and_b32_e32 v3, 0xc0, v3
	v_or3_b32 v3, v8, v3, v5
	s_lshr_b32 s28, s3, 6
	v_mad_u64_u32 v[150:151], s[0:1], s34, v4, v[2:3]
	v_mad_u64_u32 v[152:153], s[0:1], s34, v3, v[2:3]
	s_lshl_b32 s0, s28, 10
	s_add_i32 s54, s0, 0
	s_and_b32 s0, s2, 7
	s_lshl_b32 s0, s0, s50
	s_ashr_i32 s1, s2, 3
	s_add_i32 s0, s0, s1
	s_lshl_b32 s30, -1, s51
	s_ashr_i32 s1, s0, s51
	s_andn2_b32 s0, s0, s30
	s_lshl_b32 s1, s1, 3
	s_and_b32 s28, s0, 7
	s_ashr_i32 s35, s34, 31
	s_ff1_i32_b32 s52, s5
	s_or_b32 s77, s1, s28
	s_bfe_u32 s4, s3, 0x20006
	s_lshr_b32 s15, s3, 8
	s_lshl_b64 s[22:23], s[34:35], 7
	s_lshl_b64 s[24:25], s[34:35], 3
	s_lshl_b64 s[26:27], s[34:35], 8
	s_lshr_b32 s76, s0, 3
	s_ashr_i32 s0, s77, s52
	s_add_i32 s1, s5, -1
	s_cmp_lg_u32 s7, 0
	s_cselect_b32 s7, s1, -1
	s_and_b32 s5, s77, s7
	s_mul_i32 s0, s0, s6
	s_add_i32 s28, s0, s76
	s_ashr_i32 s0, s5, 31
	s_mul_i32 s0, s26, s0
	s_mul_hi_u32 s1, s26, s5
	s_add_i32 s29, s1, s0
	s_lshr_b64 s[0:1], s[34:35], 24
	s_mul_i32 s1, s0, s5
	s_add_i32 s31, s29, s1
	s_ashr_i32 s29, s28, 31
	s_mul_i32 s36, s26, s5
	s_mul_i32 s1, s26, s29
	s_mul_hi_u32 s5, s26, s28
	s_add_i32 s1, s5, s1
	s_mul_i32 s0, s0, s28
	s_add_i32 s1, s1, s0
	s_mul_i32 s0, s26, s28
	s_add_u32 s38, s18, s0
	v_bfe_u32 v1, v0, 4, 2
	s_addc_u32 s39, s19, s1
	s_lshl_b64 s[0:1], s[28:29], 10
	v_lshlrev_b32_e32 v2, 6, v1
	s_add_u32 s0, s10, s0
	v_lshl_or_b32 v147, s4, 8, v2
	s_addc_u32 s1, s11, s1
	global_load_dwordx4 v[14:17], v147, s[0:1]
	global_load_dwordx4 v[10:13], v147, s[0:1] offset:16
	global_load_dwordx4 v[6:9], v147, s[0:1] offset:32
	global_load_dwordx4 v[2:5], v147, s[0:1] offset:48
	s_add_i32 s55, s54, 0x10000
	s_mov_b32 m0, s55
	s_nop 0
	global_load_lds_dwordx4 v148, s[38:39]
	s_add_i32 s56, s54, 0x12000
	s_mov_b32 m0, s56
	s_nop 0
	global_load_lds_dwordx4 v152, s[38:39]
	s_add_u32 s40, s16, s36
	s_addc_u32 s41, s17, s31
	s_mov_b32 m0, s54
	s_nop 0
	global_load_lds_dwordx4 v146, s[40:41]
	s_add_i32 s57, s54, 0x2000
	s_add_i32 s58, s54, 0x14000
	s_mov_b32 m0, s57
	s_nop 0
	global_load_lds_dwordx4 v150, s[40:41]
	s_add_u32 s0, s38, s24
	s_addc_u32 s1, s39, s25
	s_mov_b32 m0, s58
	s_nop 0
	global_load_lds_dwordx4 v148, s[0:1]
	s_add_i32 s59, s54, 0x16000
	s_add_i32 s60, s54, 0x4000
	s_mov_b32 m0, s59
	s_nop 0
	global_load_lds_dwordx4 v152, s[0:1]
	s_add_u32 s36, s40, s22
	s_addc_u32 s37, s41, s23
	s_mov_b32 m0, s60
	s_nop 0
	global_load_lds_dwordx4 v146, s[36:37]
	s_add_i32 s61, s54, 0x6000
	s_mov_b32 m0, s61
	s_nop 0
	global_load_lds_dwordx4 v150, s[36:37]
	s_mov_b32 s53, 0
	s_mov_b32 s5, 0x10000
	s_cmp_lg_u32 s15, 1
	s_cbranch_scc1 .LBB4_3
.LBB4_3:
	s_lshr_b32 s29, s35, 25
	s_add_i32 s29, s34, s29
	s_not_b32 s62, s30
	s_ashr_i32 s63, s29, 7
	s_add_i32 s64, s54, 0x18000
	v_and_b32_e32 v19, 15, v0
	v_and_b32_e32 v0, 4, v0
	s_add_u32 s30, s38, 0x80
	v_lshl_or_b32 v149, s15, 6, v19
	v_lshlrev_b32_e32 v20, 5, v1
	v_and_or_b32 v0, v18, 1, v0
	s_waitcnt vmcnt(4)
	s_barrier
	s_addc_u32 s31, s39, 0
	s_mov_b32 m0, s64
	s_nop 0
	global_load_lds_dwordx4 v148, s[30:31]
	s_add_i32 s65, s54, 0x1a000
	s_add_i32 s66, s54, 0x8000
	v_lshlrev_b32_e32 v21, 7, v149
	v_lshlrev_b32_e32 v0, 4, v0
	v_or_b32_e32 v23, 16, v20
	s_mov_b32 m0, s65
	s_nop 0
	global_load_lds_dwordx4 v152, s[30:31]
	s_add_u32 s30, s40, 0x80
	v_xor_b32_e32 v18, v0, v20
	v_bitop3_b32 v22, v21, v0, v20 bitop3:0xf6
	v_bitop3_b32 v20, v0, v20, 16 bitop3:0x1e
	v_bitop3_b32 v21, v21, v0, v23 bitop3:0xf6
	v_lshlrev_b32_e32 v0, 7, v19
	s_addc_u32 s31, s41, 0
	s_mov_b32 m0, s66
	s_nop 0
	global_load_lds_dwordx4 v146, s[30:31]
	s_add_i32 s67, s54, 0xa000
	s_add_i32 s68, s54, 0x1c000
	v_lshl_or_b32 v0, s4, 12, v0
	s_mov_b32 m0, s67
	s_nop 0
	global_load_lds_dwordx4 v150, s[30:31]
	s_add_u32 s0, s0, 0x80
	v_or3_b32 v18, v18, v0, s5
	v_or3_b32 v19, v20, v0, s5
	s_addc_u32 s1, s1, 0
	s_mov_b32 m0, s68
	s_nop 0
	global_load_lds_dwordx4 v148, s[0:1]
	v_lshlrev_b32_e32 v0, 4, v1
	s_add_i32 s69, s54, 0x1e000
	s_mov_b32 m0, s69
	s_nop 0
	global_load_lds_dwordx4 v152, s[0:1]
	v_and_b32_e32 v1, 32, v0
	v_and_b32_e32 v153, 16, v0
	v_or_b32_e32 v158, 32, v0
	v_div_scale_f32 v0, s[0:1], s13, s13, 1.0
	v_lshl_or_b32 v151, s4, 6, v1
	v_rcp_f32_e32 v1, v0
	s_cmpk_gt_i32 s34, 0x7f
	s_cselect_b64 s[30:31], -1, 0
	s_add_i32 s70, s54, 0xc000
	v_fma_f32 v20, -v0, v1, 1.0
	v_fmac_f32_e32 v1, v20, v1
	v_div_scale_f32 v20, vcc, 1.0, s13, 1.0
	v_mul_f32_e32 v23, v20, v1
	v_fma_f32 v24, -v0, v23, v20
	v_fmac_f32_e32 v23, v24, v1
	v_fma_f32 v0, -v0, v23, v20
	v_div_fmas_f32 v0, v0, v1, v23
	v_mov_b32_e32 v1, s14
	v_mul_f32_e32 v1, s13, v1
	v_div_scale_f32 v20, s[0:1], v1, v1, 1.0
	v_rcp_f32_e32 v23, v20
	s_add_i32 s71, s54, 0xe000
	s_ashr_i32 s72, s33, 31
	s_ashr_i32 s73, s2, 31
	v_fma_f32 v24, -v20, v23, 1.0
	v_fmac_f32_e32 v23, v24, v23
	v_div_scale_f32 v24, vcc, 1.0, v1, 1.0
	v_mul_f32_e32 v25, v24, v23
	v_fma_f32 v26, -v20, v25, v24
	v_fmac_f32_e32 v25, v26, v23
	v_fma_f32 v20, -v20, v25, v24
	s_waitcnt vmcnt(6)
	v_div_fmas_f32 v20, v20, v23, v25
	s_cmp_eq_u32 s63, 2
	v_div_fixup_f32 v0, v0, s13, 1.0
	v_div_fixup_f32 v159, v20, v1, 1.0
	s_cselect_b64 s[14:15], -1, 0
	s_cmpk_gt_u32 s34, 0x17f
	v_mov_b32_e32 v154, v0
	v_mov_b32_e32 v155, v0
	v_mul_f32_e32 v160, 0x40c00000, v159
	s_cselect_b64 s[34:35], -1, 0
	v_add_u32_e32 v161, 0, v18
	v_add_u32_e32 v162, 0, v19
	v_add_u32_e32 v163, 0, v22
	v_add_u32_e32 v164, 0, v21
	s_barrier
	s_branch .LBB4_5
.LBB4_4:
	s_cmpk_gt_u32 s3, 0xff
	s_cbranch_scc1 .Lrs_b_4
	s_barrier
.Lrs_b_4:
	v_med3_f32 v166, v18, v160, 0
	v_med3_f32 v165, v19, v160, 0
	v_med3_f32 v167, v20, v160, 0
	v_med3_f32 v168, v21, v160, 0
	v_cvt_scalef32_pk_fp4_f32 v166, v166, v165, v159
	v_med3_f32 v169, v22, v160, 0
	v_med3_f32 v170, v23, v160, 0
	v_cvt_scalef32_pk_fp4_f32 v166, v167, v168, v159 op_sel:[0,0,1,0]
	v_med3_f32 v167, v50, v160, 0
	v_med3_f32 v165, v51, v160, 0
	v_med3_f32 v171, v24, v160, 0
	v_med3_f32 v172, v25, v160, 0
	v_cvt_scalef32_pk_fp4_f32 v166, v169, v170, v159 op_sel:[0,0,0,1]
	v_med3_f32 v168, v52, v160, 0
	v_med3_f32 v169, v53, v160, 0
	v_cvt_scalef32_pk_fp4_f32 v167, v167, v165, v159
	v_cvt_scalef32_pk_fp4_f32 v166, v171, v172, v159 op_sel:[0,0,1,1]
	v_med3_f32 v170, v54, v160, 0
	v_med3_f32 v171, v55, v160, 0
	v_cvt_scalef32_pk_fp4_f32 v167, v168, v169, v159 op_sel:[0,0,1,0]
	v_med3_f32 v168, v26, v160, 0
	v_med3_f32 v165, v27, v160, 0
	v_med3_f32 v172, v56, v160, 0
	v_med3_f32 v173, v57, v160, 0
	v_cvt_scalef32_pk_fp4_f32 v167, v170, v171, v159 op_sel:[0,0,0,1]
	v_med3_f32 v169, v28, v160, 0
	v_med3_f32 v170, v29, v160, 0
	v_cvt_scalef32_pk_fp4_f32 v168, v168, v165, v159
	v_cvt_scalef32_pk_fp4_f32 v167, v172, v173, v159 op_sel:[0,0,1,1]
	v_med3_f32 v171, v30, v160, 0
	v_med3_f32 v172, v31, v160, 0
	v_cvt_scalef32_pk_fp4_f32 v168, v169, v170, v159 op_sel:[0,0,1,0]
	v_med3_f32 v169, v58, v160, 0
	v_med3_f32 v165, v59, v160, 0
	v_med3_f32 v173, v32, v160, 0
	v_med3_f32 v174, v33, v160, 0
	v_cvt_scalef32_pk_fp4_f32 v168, v171, v172, v159 op_sel:[0,0,0,1]
	v_med3_f32 v170, v60, v160, 0
	v_med3_f32 v171, v61, v160, 0
	v_cvt_scalef32_pk_fp4_f32 v169, v169, v165, v159
	v_lshl_add_u32 v1, s77, 8, v149
	v_lshl_or_b32 v156, s76, 8, v151
	v_cvt_scalef32_pk_fp4_f32 v168, v173, v174, v159 op_sel:[0,0,1,1]
	v_med3_f32 v172, v62, v160, 0
	v_med3_f32 v173, v63, v160, 0
	v_cvt_scalef32_pk_fp4_f32 v169, v170, v171, v159 op_sel:[0,0,1,0]
	v_ashrrev_i32_e32 v156, 1, v156
	v_med3_f32 v174, v64, v160, 0
	v_med3_f32 v175, v65, v160, 0
	v_cvt_scalef32_pk_fp4_f32 v169, v172, v173, v159 op_sel:[0,0,0,1]
	v_or_b32_e32 v165, v1, v153
	v_mov_b64_e32 v[170:171], s[8:9]
	v_ashrrev_i32_e32 v157, 31, v156
	v_cvt_scalef32_pk_fp4_f32 v169, v174, v175, v159 op_sel:[0,0,1,1]
	v_mad_i64_i32 v[172:173], s[38:39], v165, s12, v[170:171]
	v_permlane16_swap_b32_e32 v166, v168
	v_permlane16_swap_b32_e32 v167, v169
	v_lshl_add_u64 v[172:173], v[172:173], 0, v[156:157]
	global_store_dwordx4 v[172:173], v[166:169], off
	v_med3_f32 v165, v35, v160, 0
	v_med3_f32 v172, v39, v160, 0
	v_med3_f32 v166, v34, v160, 0
	v_med3_f32 v167, v36, v160, 0
	v_med3_f32 v168, v37, v160, 0
	v_cvt_scalef32_pk_fp4_f32 v166, v166, v165, v159
	v_med3_f32 v169, v38, v160, 0
	v_cvt_scalef32_pk_fp4_f32 v166, v167, v168, v159 op_sel:[0,0,1,0]
	v_med3_f32 v167, v66, v160, 0
	v_med3_f32 v165, v67, v160, 0
	v_med3_f32 v173, v40, v160, 0
	v_med3_f32 v174, v41, v160, 0
	v_cvt_scalef32_pk_fp4_f32 v166, v169, v172, v159 op_sel:[0,0,0,1]
	v_med3_f32 v168, v68, v160, 0
	v_med3_f32 v169, v69, v160, 0
	v_cvt_scalef32_pk_fp4_f32 v167, v167, v165, v159
	v_cvt_scalef32_pk_fp4_f32 v166, v173, v174, v159 op_sel:[0,0,1,1]
	v_med3_f32 v172, v70, v160, 0
	v_med3_f32 v173, v71, v160, 0
	v_cvt_scalef32_pk_fp4_f32 v167, v168, v169, v159 op_sel:[0,0,1,0]
	v_med3_f32 v168, v42, v160, 0
	v_med3_f32 v165, v43, v160, 0
	v_med3_f32 v174, v72, v160, 0
	v_med3_f32 v175, v73, v160, 0
	v_cvt_scalef32_pk_fp4_f32 v167, v172, v173, v159 op_sel:[0,0,0,1]
	v_med3_f32 v169, v44, v160, 0
	v_med3_f32 v172, v45, v160, 0
	v_cvt_scalef32_pk_fp4_f32 v168, v168, v165, v159
	v_cvt_scalef32_pk_fp4_f32 v167, v174, v175, v159 op_sel:[0,0,1,1]
	v_med3_f32 v173, v46, v160, 0
	v_med3_f32 v174, v47, v160, 0
	v_cvt_scalef32_pk_fp4_f32 v168, v169, v172, v159 op_sel:[0,0,1,0]
	v_med3_f32 v169, v74, v160, 0
	v_med3_f32 v165, v75, v160, 0
	v_med3_f32 v175, v48, v160, 0
	v_med3_f32 v176, v49, v160, 0
	v_cvt_scalef32_pk_fp4_f32 v168, v173, v174, v159 op_sel:[0,0,0,1]
	v_med3_f32 v172, v76, v160, 0
	v_med3_f32 v173, v77, v160, 0
	v_cvt_scalef32_pk_fp4_f32 v169, v169, v165, v159
	v_cvt_scalef32_pk_fp4_f32 v168, v175, v176, v159 op_sel:[0,0,1,1]
	v_med3_f32 v174, v78, v160, 0
	v_med3_f32 v175, v79, v160, 0
	v_cvt_scalef32_pk_fp4_f32 v169, v172, v173, v159 op_sel:[0,0,1,0]
	v_med3_f32 v176, v80, v160, 0
	v_med3_f32 v177, v81, v160, 0
	v_cvt_scalef32_pk_fp4_f32 v169, v174, v175, v159 op_sel:[0,0,0,1]
	v_or_b32_e32 v165, v1, v158
	v_cvt_scalef32_pk_fp4_f32 v169, v176, v177, v159 op_sel:[0,0,1,1]
	v_mad_i64_i32 v[172:173], s[38:39], v165, s12, v[170:171]
	v_permlane16_swap_b32_e32 v166, v168
	v_permlane16_swap_b32_e32 v167, v169
	v_lshl_add_u64 v[172:173], v[172:173], 0, v[156:157]
	global_store_dwordx4 v[172:173], v[166:169], off
	v_med3_f32 v165, v87, v160, 0
	v_med3_f32 v172, v91, v160, 0
	v_med3_f32 v166, v86, v160, 0
	v_med3_f32 v167, v88, v160, 0
	v_med3_f32 v168, v89, v160, 0
	v_cvt_scalef32_pk_fp4_f32 v166, v166, v165, v159
	v_med3_f32 v169, v90, v160, 0
	v_cvt_scalef32_pk_fp4_f32 v166, v167, v168, v159 op_sel:[0,0,1,0]
	v_med3_f32 v167, v94, v160, 0
	v_med3_f32 v165, v95, v160, 0
	v_med3_f32 v173, v92, v160, 0
	v_med3_f32 v174, v93, v160, 0
	v_cvt_scalef32_pk_fp4_f32 v166, v169, v172, v159 op_sel:[0,0,0,1]
	v_med3_f32 v168, v96, v160, 0
	v_med3_f32 v169, v97, v160, 0
	v_cvt_scalef32_pk_fp4_f32 v167, v167, v165, v159
	v_cvt_scalef32_pk_fp4_f32 v166, v173, v174, v159 op_sel:[0,0,1,1]
	v_med3_f32 v172, v102, v160, 0
	v_med3_f32 v173, v103, v160, 0
	v_cvt_scalef32_pk_fp4_f32 v167, v168, v169, v159 op_sel:[0,0,1,0]
	v_med3_f32 v168, v98, v160, 0
	v_med3_f32 v165, v99, v160, 0
	v_med3_f32 v174, v104, v160, 0
	v_med3_f32 v175, v105, v160, 0
	v_cvt_scalef32_pk_fp4_f32 v167, v172, v173, v159 op_sel:[0,0,0,1]
	v_med3_f32 v169, v100, v160, 0
	v_med3_f32 v172, v101, v160, 0
	v_cvt_scalef32_pk_fp4_f32 v168, v168, v165, v159
	v_cvt_scalef32_pk_fp4_f32 v167, v174, v175, v159 op_sel:[0,0,1,1]
	v_med3_f32 v173, v106, v160, 0
	v_med3_f32 v174, v107, v160, 0
	v_cvt_scalef32_pk_fp4_f32 v168, v169, v172, v159 op_sel:[0,0,1,0]
	v_med3_f32 v169, v110, v160, 0
	v_med3_f32 v165, v111, v160, 0
	v_med3_f32 v175, v108, v160, 0
	v_med3_f32 v176, v109, v160, 0
	v_cvt_scalef32_pk_fp4_f32 v168, v173, v174, v159 op_sel:[0,0,0,1]
	v_med3_f32 v172, v112, v160, 0
	v_med3_f32 v173, v113, v160, 0
	v_cvt_scalef32_pk_fp4_f32 v169, v169, v165, v159
	v_add_u32_e32 v1, 0x80, v1
	v_cvt_scalef32_pk_fp4_f32 v168, v175, v176, v159 op_sel:[0,0,1,1]
	v_med3_f32 v174, v114, v160, 0
	v_med3_f32 v175, v115, v160, 0
	v_cvt_scalef32_pk_fp4_f32 v169, v172, v173, v159 op_sel:[0,0,1,0]
	v_med3_f32 v176, v116, v160, 0
	v_med3_f32 v177, v117, v160, 0
	v_cvt_scalef32_pk_fp4_f32 v169, v174, v175, v159 op_sel:[0,0,0,1]
	v_or_b32_e32 v165, v1, v153
	v_cvt_scalef32_pk_fp4_f32 v169, v176, v177, v159 op_sel:[0,0,1,1]
	v_mad_i64_i32 v[172:173], s[38:39], v165, s12, v[170:171]
	v_permlane16_swap_b32_e32 v166, v168
	v_permlane16_swap_b32_e32 v167, v169
	v_lshl_add_u64 v[172:173], v[172:173], 0, v[156:157]
	global_store_dwordx4 v[172:173], v[166:169], off
	v_med3_f32 v165, v119, v160, 0
	v_med3_f32 v172, v127, v160, 0
	v_med3_f32 v166, v118, v160, 0
	v_med3_f32 v167, v120, v160, 0
	v_med3_f32 v168, v121, v160, 0
	v_cvt_scalef32_pk_fp4_f32 v166, v166, v165, v159
	v_med3_f32 v169, v126, v160, 0
	v_cvt_scalef32_pk_fp4_f32 v166, v167, v168, v159 op_sel:[0,0,1,0]
	v_med3_f32 v167, v122, v160, 0
	v_med3_f32 v165, v123, v160, 0
	v_med3_f32 v173, v128, v160, 0
	v_med3_f32 v174, v129, v160, 0
	v_cvt_scalef32_pk_fp4_f32 v166, v169, v172, v159 op_sel:[0,0,0,1]
	v_med3_f32 v168, v124, v160, 0
	v_med3_f32 v169, v125, v160, 0
	v_cvt_scalef32_pk_fp4_f32 v167, v167, v165, v159
	v_cvt_scalef32_pk_fp4_f32 v166, v173, v174, v159 op_sel:[0,0,1,1]
	v_med3_f32 v172, v130, v160, 0
	v_med3_f32 v173, v131, v160, 0
	v_cvt_scalef32_pk_fp4_f32 v167, v168, v169, v159 op_sel:[0,0,1,0]
	v_med3_f32 v168, v138, v160, 0
	v_med3_f32 v165, v139, v160, 0
	v_med3_f32 v174, v132, v160, 0
	v_med3_f32 v175, v133, v160, 0
	v_cvt_scalef32_pk_fp4_f32 v167, v172, v173, v159 op_sel:[0,0,0,1]
	v_med3_f32 v169, v140, v160, 0
	v_med3_f32 v172, v141, v160, 0
	v_cvt_scalef32_pk_fp4_f32 v168, v168, v165, v159
	v_cvt_scalef32_pk_fp4_f32 v167, v174, v175, v159 op_sel:[0,0,1,1]
	v_med3_f32 v173, v82, v160, 0
	v_med3_f32 v174, v83, v160, 0
	v_cvt_scalef32_pk_fp4_f32 v168, v169, v172, v159 op_sel:[0,0,1,0]
	v_med3_f32 v169, v134, v160, 0
	v_med3_f32 v165, v135, v160, 0
	v_med3_f32 v175, v84, v160, 0
	v_med3_f32 v176, v85, v160, 0
	v_cvt_scalef32_pk_fp4_f32 v168, v173, v174, v159 op_sel:[0,0,0,1]
	v_med3_f32 v172, v136, v160, 0
	v_med3_f32 v173, v137, v160, 0
	v_cvt_scalef32_pk_fp4_f32 v169, v169, v165, v159
	v_cvt_scalef32_pk_fp4_f32 v168, v175, v176, v159 op_sel:[0,0,1,1]
	v_med3_f32 v174, v142, v160, 0
	v_med3_f32 v175, v143, v160, 0
	v_cvt_scalef32_pk_fp4_f32 v169, v172, v173, v159 op_sel:[0,0,1,0]
	v_med3_f32 v176, v144, v160, 0
	v_med3_f32 v177, v145, v160, 0
	v_cvt_scalef32_pk_fp4_f32 v169, v174, v175, v159 op_sel:[0,0,0,1]
	v_or_b32_e32 v1, v1, v158
	v_cvt_scalef32_pk_fp4_f32 v169, v176, v177, v159 op_sel:[0,0,1,1]
	v_mad_i64_i32 v[170:171], s[38:39], v1, s12, v[170:171]
	v_permlane16_swap_b32_e32 v166, v168
	v_permlane16_swap_b32_e32 v167, v169
	v_lshl_add_u64 v[156:157], v[170:171], 0, v[156:157]
	s_mov_b32 s76, s13
	s_mov_b32 s77, s74
	s_mov_b64 s[38:39], s[4:5]
	s_mov_b64 s[40:41], s[36:37]
	s_mov_b64 vcc, s[0:1]
	global_store_dwordx4 v[156:157], v[166:169], off
	s_cbranch_vccnz .LBB4_17

.LBB4_12:
	s_cmpk_gt_u32 s3, 0xff
	s_cbranch_scc0 .Lrs_a_4
	s_barrier

.LBB4_17:
	s_waitcnt vmcnt(0)
	s_cmpk_gt_u32 s3, 0xff
	s_cbranch_scc1 .LBB4_19
.LBB4_19:
	s_barrier

_Z6k_gemmI4Epi8ILi1ELb1ELb1EEEv4GemmT_iiii:
	s_load_dwordx4 s[4:7], s[0:1], 0x38
	s_waitcnt lgkmcnt(0)
	s_mul_i32 s3, s5, s4
	s_mul_i32 s20, s3, s6
	s_cmp_ge_i32 s2, s20
	v_readfirstlane_b32 s3, v0
	s_cbranch_scc1 .LBB5_20
	s_ashr_i32 s21, s20, 31
	s_load_dword s34, s[0:1], 0x10
	s_load_dwordx4 s[16:19], s[0:1], 0x0
	s_load_dwordx8 s[8:15], s[0:1], 0x18
	s_load_dword s33, s[0:1], 0x48
	s_lshr_b32 s0, s21, 29
	v_lshrrev_b32_e32 v5, 5, v0
	s_add_i32 s0, s20, s0
	v_lshlrev_b32_e32 v3, 4, v0
	v_and_b32_e32 v5, 4, v5
	v_lshrrev_b32_e32 v6, 3, v0
	v_lshrrev_b32_e32 v7, 2, v0
	v_lshrrev_b32_e32 v18, 1, v0
	v_lshlrev_b32_e32 v9, 1, v0
	s_ashr_i32 s0, s0, 3
	v_and_b32_e32 v2, 16, v0
	v_and_b32_e32 v4, 0x70, v3
	v_and_b32_e32 v7, 64, v7
	v_and_or_b32 v5, v6, 3, v5
	v_and_b32_e32 v8, 48, v18
	v_and_b32_e32 v9, 64, v9
	s_ff1_i32_b32 s37, s0
	s_lshl_b32 s0, s6, 3
	v_or3_b32 v7, v8, v7, v5
	v_bitop3_b32 v2, v9, v4, v2 bitop3:0x36
	s_ff1_i32_b32 s52, s0
	s_waitcnt lgkmcnt(0)
	v_mad_u64_u32 v[146:147], s[0:1], s34, v6, v[2:3]
	v_mad_u64_u32 v[148:149], s[0:1], s34, v7, v[2:3]
	v_or_b32_e32 v3, 0x2000, v3
	v_lshrrev_b32_e32 v4, 7, v3
	v_lshrrev_b32_e32 v3, 6, v3
	v_and_b32_e32 v3, 0xc0, v3
	v_or3_b32 v3, v8, v3, v5
	s_lshr_b32 s28, s3, 6
	v_mad_u64_u32 v[150:151], s[0:1], s34, v4, v[2:3]
	v_mad_u64_u32 v[152:153], s[0:1], s34, v3, v[2:3]
	s_lshl_b32 s0, s28, 10
	s_add_i32 s55, s0, 0
	s_and_b32 s0, s2, 7
	s_lshl_b32 s0, s0, s37
	s_ashr_i32 s1, s2, 3
	s_add_i32 s0, s0, s1
	s_lshl_b32 s30, -1, s52
	s_ashr_i32 s1, s0, s52
	s_andn2_b32 s0, s0, s30
	s_lshl_b32 s1, s1, 3
	s_and_b32 s28, s0, 7
	s_ashr_i32 s35, s34, 31
	s_ff1_i32_b32 s53, s5
	s_or_b32 s78, s1, s28
	s_bfe_u32 s4, s3, 0x20006
	s_lshr_b32 s15, s3, 8
	s_lshl_b64 s[22:23], s[34:35], 7
	s_lshl_b64 s[24:25], s[34:35], 3
	s_lshl_b64 s[26:27], s[34:35], 8
	s_lshr_b32 s77, s0, 3
	s_ashr_i32 s0, s78, s53
	s_add_i32 s1, s5, -1
	s_cmp_lg_u32 s7, 0
	s_cselect_b32 s7, s1, -1
	s_and_b32 s5, s78, s7
	s_mul_i32 s0, s0, s6
	s_add_i32 s28, s0, s77
	s_ashr_i32 s0, s5, 31
	s_mul_i32 s0, s26, s0
	s_mul_hi_u32 s1, s26, s5
	s_add_i32 s29, s1, s0
	s_lshr_b64 s[0:1], s[34:35], 24
	s_mul_i32 s1, s0, s5
	s_add_i32 s31, s29, s1
	s_ashr_i32 s29, s28, 31
	s_mul_i32 s36, s26, s5
	s_mul_i32 s1, s26, s29
	s_mul_hi_u32 s5, s26, s28
	s_add_i32 s1, s5, s1
	s_mul_i32 s0, s0, s28
	s_add_i32 s1, s1, s0
	s_mul_i32 s0, s26, s28
	s_add_u32 s40, s18, s0
	v_bfe_u32 v1, v0, 4, 2
	s_addc_u32 s41, s19, s1
	s_lshl_b64 s[0:1], s[28:29], 10
	v_lshlrev_b32_e32 v2, 6, v1
	s_add_u32 s0, s10, s0
	v_lshl_or_b32 v147, s4, 8, v2
	s_addc_u32 s1, s11, s1
	global_load_dwordx4 v[14:17], v147, s[0:1]
	global_load_dwordx4 v[10:13], v147, s[0:1] offset:16
	global_load_dwordx4 v[6:9], v147, s[0:1] offset:32
	global_load_dwordx4 v[2:5], v147, s[0:1] offset:48
	s_add_i32 s56, s55, 0x10000
	s_mov_b32 m0, s56
	s_nop 0
	global_load_lds_dwordx4 v148, s[40:41]
	s_add_i32 s57, s55, 0x12000
	s_mov_b32 m0, s57
	s_nop 0
	global_load_lds_dwordx4 v152, s[40:41]
	s_add_u32 s42, s16, s36
	s_addc_u32 s43, s17, s31
	s_mov_b32 m0, s55
	s_nop 0
	global_load_lds_dwordx4 v146, s[42:43]
	s_add_i32 s58, s55, 0x2000
	s_add_i32 s59, s55, 0x14000
	s_mov_b32 m0, s58
	s_nop 0
	global_load_lds_dwordx4 v150, s[42:43]
	s_add_u32 s0, s40, s24
	s_addc_u32 s1, s41, s25
	s_mov_b32 m0, s59
	s_nop 0
	global_load_lds_dwordx4 v148, s[0:1]
	s_add_i32 s60, s55, 0x16000
	s_add_i32 s61, s55, 0x4000
	s_mov_b32 m0, s60
	s_nop 0
	global_load_lds_dwordx4 v152, s[0:1]
	s_add_u32 s38, s42, s22
	s_addc_u32 s39, s43, s23
	s_mov_b32 m0, s61
	s_nop 0
	global_load_lds_dwordx4 v146, s[38:39]
	s_add_i32 s62, s55, 0x6000
	s_mov_b32 m0, s62
	s_nop 0
	global_load_lds_dwordx4 v150, s[38:39]
	s_mov_b32 s54, 0
	s_mov_b32 s5, 0x10000
	s_cmp_lg_u32 s15, 1
	s_cbranch_scc1 .LBB5_3
.LBB5_3:
	s_lshr_b32 s29, s35, 25
	s_add_i32 s29, s34, s29
	s_not_b32 s63, s30
	s_ashr_i32 s64, s29, 7
	s_add_i32 s65, s55, 0x18000
	v_and_b32_e32 v19, 15, v0
	v_and_b32_e32 v0, 4, v0
	s_add_u32 s30, s40, 0x80
	v_lshl_or_b32 v149, s15, 6, v19
	v_lshlrev_b32_e32 v20, 5, v1
	v_and_or_b32 v0, v18, 1, v0
	s_waitcnt vmcnt(4)
	s_barrier
	s_addc_u32 s31, s41, 0
	s_mov_b32 m0, s65
	s_nop 0
	global_load_lds_dwordx4 v148, s[30:31]
	s_add_i32 s66, s55, 0x1a000
	s_add_i32 s67, s55, 0x8000
	v_lshlrev_b32_e32 v21, 7, v149
	v_lshlrev_b32_e32 v0, 4, v0
	v_or_b32_e32 v23, 16, v20
	s_mov_b32 m0, s66
	s_nop 0
	global_load_lds_dwordx4 v152, s[30:31]
	s_add_u32 s30, s42, 0x80
	v_xor_b32_e32 v18, v0, v20
	v_bitop3_b32 v22, v21, v0, v20 bitop3:0xf6
	v_bitop3_b32 v20, v0, v20, 16 bitop3:0x1e
	v_bitop3_b32 v21, v21, v0, v23 bitop3:0xf6
	v_lshlrev_b32_e32 v0, 7, v19
	s_addc_u32 s31, s43, 0
	s_mov_b32 m0, s67
	s_nop 0
	global_load_lds_dwordx4 v146, s[30:31]
	s_add_i32 s68, s55, 0xa000
	s_add_i32 s69, s55, 0x1c000
	v_lshl_or_b32 v0, s4, 12, v0
	s_mov_b32 m0, s68
	s_nop 0
	global_load_lds_dwordx4 v150, s[30:31]
	s_add_u32 s0, s0, 0x80
	v_or3_b32 v18, v18, v0, s5
	v_or3_b32 v19, v20, v0, s5
	s_addc_u32 s1, s1, 0
	s_mov_b32 m0, s69
	s_nop 0
	global_load_lds_dwordx4 v148, s[0:1]
	v_lshlrev_b32_e32 v0, 4, v1
	s_add_i32 s70, s55, 0x1e000
	s_mov_b32 m0, s70
	s_nop 0
	global_load_lds_dwordx4 v152, s[0:1]
	v_and_b32_e32 v1, 32, v0
	v_and_b32_e32 v153, 16, v0
	v_or_b32_e32 v160, 32, v0
	v_div_scale_f32 v0, s[0:1], s13, s13, 1.0
	v_lshl_or_b32 v151, s4, 6, v1
	v_rcp_f32_e32 v1, v0
	s_cmpk_gt_i32 s34, 0x7f
	s_cselect_b64 s[30:31], -1, 0
	s_add_i32 s71, s55, 0xc000
	v_fma_f32 v20, -v0, v1, 1.0
	v_fmac_f32_e32 v1, v20, v1
	v_div_scale_f32 v20, vcc, 1.0, s13, 1.0
	v_mul_f32_e32 v23, v20, v1
	v_fma_f32 v24, -v0, v23, v20
	v_fmac_f32_e32 v23, v24, v1
	v_fma_f32 v0, -v0, v23, v20
	v_div_fmas_f32 v0, v0, v1, v23
	v_mov_b32_e32 v1, s14
	v_mul_f32_e32 v1, s13, v1
	v_div_scale_f32 v20, s[0:1], v1, v1, 1.0
	v_rcp_f32_e32 v23, v20
	s_add_i32 s72, s55, 0xe000
	s_ashr_i32 s73, s33, 31
	s_ashr_i32 s74, s2, 31
	v_fma_f32 v24, -v20, v23, 1.0
	v_fmac_f32_e32 v23, v24, v23
	v_div_scale_f32 v24, vcc, 1.0, v1, 1.0
	v_mul_f32_e32 v25, v24, v23
	v_fma_f32 v26, -v20, v25, v24
	v_fmac_f32_e32 v25, v26, v23
	v_fma_f32 v20, -v20, v25, v24
	s_waitcnt vmcnt(6)
	v_div_fmas_f32 v20, v20, v23, v25
	s_cmp_eq_u32 s64, 2
	v_div_fixup_f32 v0, v0, s13, 1.0
	v_div_fixup_f32 v161, v20, v1, 1.0
	s_cselect_b64 s[14:15], -1, 0
	s_cmpk_gt_u32 s34, 0x17f
	v_mov_b32_e32 v154, v0
	v_mov_b32_e32 v155, v0
	v_mul_f32_e32 v162, 0x40c00000, v161
	s_cselect_b64 s[34:35], -1, 0
	s_mov_b32 s36, 0x3c23d70a
	v_add_u32_e32 v163, 0, v18
	v_add_u32_e32 v164, 0, v19
	v_add_u32_e32 v165, 0, v22
	v_add_u32_e32 v166, 0, v21
	s_barrier
	s_branch .LBB5_5

.Lrs_b_5:
	v_pk_mul_f32 v[158:159], v[18:19], s[36:37] op_sel_hi:[1,0]
	v_pk_mul_f32 v[170:171], v[20:21], s[36:37] op_sel_hi:[1,0]
	v_med3_f32 v168, v18, v158, v162
	v_med3_f32 v167, v19, v159, v162
	v_med3_f32 v169, v20, v170, v162
	v_med3_f32 v172, v21, v171, v162
	v_pk_mul_f32 v[158:159], v[22:23], s[36:37] op_sel_hi:[1,0]
	v_cvt_scalef32_pk_fp4_f32 v168, v168, v167, v161
	v_pk_mul_f32 v[170:171], v[24:25], s[36:37] op_sel_hi:[1,0]
	v_med3_f32 v158, v22, v158, v162
	v_med3_f32 v159, v23, v159, v162
	v_cvt_scalef32_pk_fp4_f32 v168, v169, v172, v161 op_sel:[0,0,1,0]
	v_med3_f32 v170, v24, v170, v162
	v_med3_f32 v171, v25, v171, v162
	v_cvt_scalef32_pk_fp4_f32 v168, v158, v159, v161 op_sel:[0,0,0,1]
	v_pk_mul_f32 v[158:159], v[50:51], s[36:37] op_sel_hi:[1,0]
	v_cvt_scalef32_pk_fp4_f32 v168, v170, v171, v161 op_sel:[0,0,1,1]
	v_pk_mul_f32 v[170:171], v[52:53], s[36:37] op_sel_hi:[1,0]
	v_med3_f32 v169, v50, v158, v162
	v_med3_f32 v167, v51, v159, v162
	v_med3_f32 v172, v52, v170, v162
	v_med3_f32 v173, v53, v171, v162
	v_pk_mul_f32 v[158:159], v[54:55], s[36:37] op_sel_hi:[1,0]
	v_cvt_scalef32_pk_fp4_f32 v169, v169, v167, v161
	v_pk_mul_f32 v[170:171], v[56:57], s[36:37] op_sel_hi:[1,0]
	v_med3_f32 v158, v54, v158, v162
	v_med3_f32 v159, v55, v159, v162
	v_cvt_scalef32_pk_fp4_f32 v169, v172, v173, v161 op_sel:[0,0,1,0]
	v_med3_f32 v170, v56, v170, v162
	v_med3_f32 v171, v57, v171, v162
	v_cvt_scalef32_pk_fp4_f32 v169, v158, v159, v161 op_sel:[0,0,0,1]
	v_pk_mul_f32 v[158:159], v[26:27], s[36:37] op_sel_hi:[1,0]
	v_cvt_scalef32_pk_fp4_f32 v169, v170, v171, v161 op_sel:[0,0,1,1]
	v_pk_mul_f32 v[172:173], v[28:29], s[36:37] op_sel_hi:[1,0]
	v_med3_f32 v170, v26, v158, v162
	v_med3_f32 v167, v27, v159, v162
	v_med3_f32 v171, v28, v172, v162
	v_med3_f32 v174, v29, v173, v162
	v_pk_mul_f32 v[158:159], v[30:31], s[36:37] op_sel_hi:[1,0]
	v_cvt_scalef32_pk_fp4_f32 v170, v170, v167, v161
	v_pk_mul_f32 v[172:173], v[32:33], s[36:37] op_sel_hi:[1,0]
	v_med3_f32 v158, v30, v158, v162
	v_med3_f32 v159, v31, v159, v162
	v_cvt_scalef32_pk_fp4_f32 v170, v171, v174, v161 op_sel:[0,0,1,0]
	v_med3_f32 v172, v32, v172, v162
	v_med3_f32 v173, v33, v173, v162
	v_cvt_scalef32_pk_fp4_f32 v170, v158, v159, v161 op_sel:[0,0,0,1]
	v_pk_mul_f32 v[158:159], v[58:59], s[36:37] op_sel_hi:[1,0]
	v_cvt_scalef32_pk_fp4_f32 v170, v172, v173, v161 op_sel:[0,0,1,1]
	v_pk_mul_f32 v[172:173], v[60:61], s[36:37] op_sel_hi:[1,0]
	v_med3_f32 v171, v58, v158, v162
	v_med3_f32 v167, v59, v159, v162
	v_med3_f32 v174, v60, v172, v162
	v_med3_f32 v175, v61, v173, v162
	v_pk_mul_f32 v[158:159], v[62:63], s[36:37] op_sel_hi:[1,0]
	v_cvt_scalef32_pk_fp4_f32 v171, v171, v167, v161
	v_lshl_add_u32 v1, s78, 8, v149
	v_lshl_or_b32 v156, s77, 8, v151
	v_pk_mul_f32 v[172:173], v[64:65], s[36:37] op_sel_hi:[1,0]
	v_med3_f32 v158, v62, v158, v162
	v_med3_f32 v159, v63, v159, v162
	v_cvt_scalef32_pk_fp4_f32 v171, v174, v175, v161 op_sel:[0,0,1,0]
	v_ashrrev_i32_e32 v156, 1, v156
	v_med3_f32 v172, v64, v172, v162
	v_med3_f32 v173, v65, v173, v162
	v_cvt_scalef32_pk_fp4_f32 v171, v158, v159, v161 op_sel:[0,0,0,1]
	v_or_b32_e32 v167, v1, v153
	v_mov_b64_e32 v[158:159], s[8:9]
	v_ashrrev_i32_e32 v157, 31, v156
	v_cvt_scalef32_pk_fp4_f32 v171, v172, v173, v161 op_sel:[0,0,1,1]
	v_mad_i64_i32 v[172:173], s[40:41], v167, s12, v[158:159]
	v_permlane16_swap_b32_e32 v168, v170
	v_permlane16_swap_b32_e32 v169, v171
	v_lshl_add_u64 v[172:173], v[172:173], 0, v[156:157]
	global_store_dwordx4 v[172:173], v[168:171], off
	v_pk_mul_f32 v[172:173], v[40:41], s[36:37] op_sel_hi:[1,0]
	s_mov_b32 s77, s13
	v_pk_mul_f32 v[168:169], v[34:35], s[36:37] op_sel_hi:[1,0]
	v_pk_mul_f32 v[170:171], v[36:37], s[36:37] op_sel_hi:[1,0]
	v_med3_f32 v168, v34, v168, v162
	v_med3_f32 v167, v35, v169, v162
	v_med3_f32 v169, v36, v170, v162
	v_med3_f32 v174, v37, v171, v162
	v_pk_mul_f32 v[170:171], v[38:39], s[36:37] op_sel_hi:[1,0]
	v_cvt_scalef32_pk_fp4_f32 v168, v168, v167, v161
	v_med3_f32 v170, v38, v170, v162
	v_med3_f32 v171, v39, v171, v162
	v_cvt_scalef32_pk_fp4_f32 v168, v169, v174, v161 op_sel:[0,0,1,0]
	v_med3_f32 v172, v40, v172, v162
	v_med3_f32 v173, v41, v173, v162
	v_cvt_scalef32_pk_fp4_f32 v168, v170, v171, v161 op_sel:[0,0,0,1]
	v_pk_mul_f32 v[170:171], v[66:67], s[36:37] op_sel_hi:[1,0]
	v_cvt_scalef32_pk_fp4_f32 v168, v172, v173, v161 op_sel:[0,0,1,1]
	v_pk_mul_f32 v[172:173], v[68:69], s[36:37] op_sel_hi:[1,0]
	v_med3_f32 v169, v66, v170, v162
	v_med3_f32 v167, v67, v171, v162
	v_med3_f32 v174, v68, v172, v162
	v_med3_f32 v175, v69, v173, v162
	v_pk_mul_f32 v[170:171], v[70:71], s[36:37] op_sel_hi:[1,0]
	v_cvt_scalef32_pk_fp4_f32 v169, v169, v167, v161
	v_pk_mul_f32 v[172:173], v[72:73], s[36:37] op_sel_hi:[1,0]
	v_med3_f32 v170, v70, v170, v162
	v_med3_f32 v171, v71, v171, v162
	v_cvt_scalef32_pk_fp4_f32 v169, v174, v175, v161 op_sel:[0,0,1,0]
	v_med3_f32 v172, v72, v172, v162
	v_med3_f32 v173, v73, v173, v162
	v_cvt_scalef32_pk_fp4_f32 v169, v170, v171, v161 op_sel:[0,0,0,1]
	v_pk_mul_f32 v[170:171], v[42:43], s[36:37] op_sel_hi:[1,0]
	v_cvt_scalef32_pk_fp4_f32 v169, v172, v173, v161 op_sel:[0,0,1,1]
	v_pk_mul_f32 v[172:173], v[44:45], s[36:37] op_sel_hi:[1,0]
	v_med3_f32 v170, v42, v170, v162
	v_med3_f32 v167, v43, v171, v162
	v_med3_f32 v171, v44, v172, v162
	v_med3_f32 v176, v45, v173, v162
	v_pk_mul_f32 v[172:173], v[46:47], s[36:37] op_sel_hi:[1,0]
	v_cvt_scalef32_pk_fp4_f32 v170, v170, v167, v161
	v_pk_mul_f32 v[174:175], v[48:49], s[36:37] op_sel_hi:[1,0]
	v_med3_f32 v172, v46, v172, v162
	v_med3_f32 v173, v47, v173, v162
	v_cvt_scalef32_pk_fp4_f32 v170, v171, v176, v161 op_sel:[0,0,1,0]
	v_med3_f32 v174, v48, v174, v162
	v_med3_f32 v175, v49, v175, v162
	v_cvt_scalef32_pk_fp4_f32 v170, v172, v173, v161 op_sel:[0,0,0,1]
	v_pk_mul_f32 v[172:173], v[74:75], s[36:37] op_sel_hi:[1,0]
	v_cvt_scalef32_pk_fp4_f32 v170, v174, v175, v161 op_sel:[0,0,1,1]
	v_pk_mul_f32 v[174:175], v[76:77], s[36:37] op_sel_hi:[1,0]
	v_med3_f32 v171, v74, v172, v162
	v_med3_f32 v167, v75, v173, v162
	v_med3_f32 v176, v76, v174, v162
	v_med3_f32 v177, v77, v175, v162
	v_pk_mul_f32 v[172:173], v[78:79], s[36:37] op_sel_hi:[1,0]
	v_cvt_scalef32_pk_fp4_f32 v171, v171, v167, v161
	v_pk_mul_f32 v[174:175], v[80:81], s[36:37] op_sel_hi:[1,0]
	v_med3_f32 v172, v78, v172, v162
	v_med3_f32 v173, v79, v173, v162
	v_cvt_scalef32_pk_fp4_f32 v171, v176, v177, v161 op_sel:[0,0,1,0]
	v_med3_f32 v174, v80, v174, v162
	v_med3_f32 v175, v81, v175, v162
	v_cvt_scalef32_pk_fp4_f32 v171, v172, v173, v161 op_sel:[0,0,0,1]
	v_or_b32_e32 v167, v1, v160
	v_cvt_scalef32_pk_fp4_f32 v171, v174, v175, v161 op_sel:[0,0,1,1]
	v_mad_i64_i32 v[172:173], s[40:41], v167, s12, v[158:159]
	v_permlane16_swap_b32_e32 v168, v170
	v_permlane16_swap_b32_e32 v169, v171
	v_lshl_add_u64 v[172:173], v[172:173], 0, v[156:157]
	global_store_dwordx4 v[172:173], v[168:171], off
	v_pk_mul_f32 v[172:173], v[92:93], s[36:37] op_sel_hi:[1,0]
	v_add_u32_e32 v1, 0x80, v1
	v_pk_mul_f32 v[168:169], v[86:87], s[36:37] op_sel_hi:[1,0]
	v_pk_mul_f32 v[170:171], v[88:89], s[36:37] op_sel_hi:[1,0]
	v_med3_f32 v168, v86, v168, v162
	v_med3_f32 v167, v87, v169, v162
	v_med3_f32 v169, v88, v170, v162
	v_med3_f32 v174, v89, v171, v162
	v_pk_mul_f32 v[170:171], v[90:91], s[36:37] op_sel_hi:[1,0]
	v_cvt_scalef32_pk_fp4_f32 v168, v168, v167, v161
	v_med3_f32 v170, v90, v170, v162
	v_med3_f32 v171, v91, v171, v162
	v_cvt_scalef32_pk_fp4_f32 v168, v169, v174, v161 op_sel:[0,0,1,0]
	v_med3_f32 v172, v92, v172, v162
	v_med3_f32 v173, v93, v173, v162
	v_cvt_scalef32_pk_fp4_f32 v168, v170, v171, v161 op_sel:[0,0,0,1]
	v_pk_mul_f32 v[170:171], v[94:95], s[36:37] op_sel_hi:[1,0]
	v_cvt_scalef32_pk_fp4_f32 v168, v172, v173, v161 op_sel:[0,0,1,1]
	v_pk_mul_f32 v[172:173], v[96:97], s[36:37] op_sel_hi:[1,0]
	v_med3_f32 v169, v94, v170, v162
	v_med3_f32 v167, v95, v171, v162
	v_med3_f32 v174, v96, v172, v162
	v_med3_f32 v175, v97, v173, v162
	v_pk_mul_f32 v[170:171], v[102:103], s[36:37] op_sel_hi:[1,0]
	v_cvt_scalef32_pk_fp4_f32 v169, v169, v167, v161
	v_pk_mul_f32 v[172:173], v[104:105], s[36:37] op_sel_hi:[1,0]
	v_med3_f32 v170, v102, v170, v162
	v_med3_f32 v171, v103, v171, v162
	v_cvt_scalef32_pk_fp4_f32 v169, v174, v175, v161 op_sel:[0,0,1,0]
	v_med3_f32 v172, v104, v172, v162
	v_med3_f32 v173, v105, v173, v162
	v_cvt_scalef32_pk_fp4_f32 v169, v170, v171, v161 op_sel:[0,0,0,1]
	v_pk_mul_f32 v[170:171], v[98:99], s[36:37] op_sel_hi:[1,0]
	v_cvt_scalef32_pk_fp4_f32 v169, v172, v173, v161 op_sel:[0,0,1,1]
	v_pk_mul_f32 v[172:173], v[100:101], s[36:37] op_sel_hi:[1,0]
	v_med3_f32 v170, v98, v170, v162
	v_med3_f32 v167, v99, v171, v162
	v_med3_f32 v171, v100, v172, v162
	v_med3_f32 v176, v101, v173, v162
	v_pk_mul_f32 v[172:173], v[106:107], s[36:37] op_sel_hi:[1,0]
	v_cvt_scalef32_pk_fp4_f32 v170, v170, v167, v161
	v_pk_mul_f32 v[174:175], v[108:109], s[36:37] op_sel_hi:[1,0]
	v_med3_f32 v172, v106, v172, v162
	v_med3_f32 v173, v107, v173, v162
	v_cvt_scalef32_pk_fp4_f32 v170, v171, v176, v161 op_sel:[0,0,1,0]
	v_med3_f32 v174, v108, v174, v162
	v_med3_f32 v175, v109, v175, v162
	v_cvt_scalef32_pk_fp4_f32 v170, v172, v173, v161 op_sel:[0,0,0,1]
	v_pk_mul_f32 v[172:173], v[110:111], s[36:37] op_sel_hi:[1,0]
	v_cvt_scalef32_pk_fp4_f32 v170, v174, v175, v161 op_sel:[0,0,1,1]
	v_pk_mul_f32 v[174:175], v[112:113], s[36:37] op_sel_hi:[1,0]
	v_med3_f32 v171, v110, v172, v162
	v_med3_f32 v167, v111, v173, v162
	v_med3_f32 v176, v112, v174, v162
	v_med3_f32 v177, v113, v175, v162
	v_pk_mul_f32 v[172:173], v[114:115], s[36:37] op_sel_hi:[1,0]
	v_cvt_scalef32_pk_fp4_f32 v171, v171, v167, v161
	v_pk_mul_f32 v[174:175], v[116:117], s[36:37] op_sel_hi:[1,0]
	v_med3_f32 v172, v114, v172, v162
	v_med3_f32 v173, v115, v173, v162
	v_cvt_scalef32_pk_fp4_f32 v171, v176, v177, v161 op_sel:[0,0,1,0]
	v_med3_f32 v174, v116, v174, v162
	v_med3_f32 v175, v117, v175, v162
	v_cvt_scalef32_pk_fp4_f32 v171, v172, v173, v161 op_sel:[0,0,0,1]
	v_or_b32_e32 v167, v1, v153
	v_cvt_scalef32_pk_fp4_f32 v171, v174, v175, v161 op_sel:[0,0,1,1]
	v_mad_i64_i32 v[172:173], s[40:41], v167, s12, v[158:159]
	v_permlane16_swap_b32_e32 v168, v170
	v_permlane16_swap_b32_e32 v169, v171
	v_lshl_add_u64 v[172:173], v[172:173], 0, v[156:157]
	global_store_dwordx4 v[172:173], v[168:171], off
	v_pk_mul_f32 v[172:173], v[128:129], s[36:37] op_sel_hi:[1,0]
	v_or_b32_e32 v1, v1, v160
	v_pk_mul_f32 v[168:169], v[118:119], s[36:37] op_sel_hi:[1,0]
	v_pk_mul_f32 v[170:171], v[120:121], s[36:37] op_sel_hi:[1,0]
	v_med3_f32 v168, v118, v168, v162
	v_med3_f32 v167, v119, v169, v162
	v_med3_f32 v169, v120, v170, v162
	v_med3_f32 v174, v121, v171, v162
	v_pk_mul_f32 v[170:171], v[126:127], s[36:37] op_sel_hi:[1,0]
	v_cvt_scalef32_pk_fp4_f32 v168, v168, v167, v161
	v_med3_f32 v170, v126, v170, v162
	v_med3_f32 v171, v127, v171, v162
	v_cvt_scalef32_pk_fp4_f32 v168, v169, v174, v161 op_sel:[0,0,1,0]
	v_med3_f32 v172, v128, v172, v162
	v_med3_f32 v173, v129, v173, v162
	v_cvt_scalef32_pk_fp4_f32 v168, v170, v171, v161 op_sel:[0,0,0,1]
	v_pk_mul_f32 v[170:171], v[122:123], s[36:37] op_sel_hi:[1,0]
	v_cvt_scalef32_pk_fp4_f32 v168, v172, v173, v161 op_sel:[0,0,1,1]
	v_pk_mul_f32 v[172:173], v[124:125], s[36:37] op_sel_hi:[1,0]
	v_med3_f32 v169, v122, v170, v162
	v_med3_f32 v167, v123, v171, v162
	v_med3_f32 v174, v124, v172, v162
	v_med3_f32 v175, v125, v173, v162
	v_pk_mul_f32 v[170:171], v[130:131], s[36:37] op_sel_hi:[1,0]
	v_cvt_scalef32_pk_fp4_f32 v169, v169, v167, v161
	v_pk_mul_f32 v[172:173], v[132:133], s[36:37] op_sel_hi:[1,0]
	v_med3_f32 v170, v130, v170, v162
	v_med3_f32 v171, v131, v171, v162
	v_cvt_scalef32_pk_fp4_f32 v169, v174, v175, v161 op_sel:[0,0,1,0]
	v_med3_f32 v172, v132, v172, v162
	v_med3_f32 v173, v133, v173, v162
	v_cvt_scalef32_pk_fp4_f32 v169, v170, v171, v161 op_sel:[0,0,0,1]
	v_pk_mul_f32 v[170:171], v[138:139], s[36:37] op_sel_hi:[1,0]
	v_cvt_scalef32_pk_fp4_f32 v169, v172, v173, v161 op_sel:[0,0,1,1]
	v_pk_mul_f32 v[172:173], v[140:141], s[36:37] op_sel_hi:[1,0]
	v_med3_f32 v170, v138, v170, v162
	v_med3_f32 v167, v139, v171, v162
	v_med3_f32 v171, v140, v172, v162
	v_med3_f32 v176, v141, v173, v162
	v_pk_mul_f32 v[172:173], v[82:83], s[36:37] op_sel_hi:[1,0]
	v_cvt_scalef32_pk_fp4_f32 v170, v170, v167, v161
	v_pk_mul_f32 v[174:175], v[84:85], s[36:37] op_sel_hi:[1,0]
	v_med3_f32 v172, v82, v172, v162
	v_med3_f32 v173, v83, v173, v162
	v_cvt_scalef32_pk_fp4_f32 v170, v171, v176, v161 op_sel:[0,0,1,0]
	v_med3_f32 v174, v84, v174, v162
	v_med3_f32 v175, v85, v175, v162
	v_cvt_scalef32_pk_fp4_f32 v170, v172, v173, v161 op_sel:[0,0,0,1]
	v_pk_mul_f32 v[172:173], v[134:135], s[36:37] op_sel_hi:[1,0]
	v_cvt_scalef32_pk_fp4_f32 v170, v174, v175, v161 op_sel:[0,0,1,1]
	v_pk_mul_f32 v[174:175], v[136:137], s[36:37] op_sel_hi:[1,0]
	v_med3_f32 v171, v134, v172, v162
	v_med3_f32 v167, v135, v173, v162
	v_med3_f32 v176, v136, v174, v162
	v_med3_f32 v177, v137, v175, v162
	v_pk_mul_f32 v[172:173], v[142:143], s[36:37] op_sel_hi:[1,0]
	v_cvt_scalef32_pk_fp4_f32 v171, v171, v167, v161
	v_pk_mul_f32 v[174:175], v[144:145], s[36:37] op_sel_hi:[1,0]
	v_med3_f32 v172, v142, v172, v162
	v_med3_f32 v173, v143, v173, v162
	v_cvt_scalef32_pk_fp4_f32 v171, v176, v177, v161 op_sel:[0,0,1,0]
	v_med3_f32 v174, v144, v174, v162
	v_med3_f32 v175, v145, v175, v162
	v_cvt_scalef32_pk_fp4_f32 v171, v172, v173, v161 op_sel:[0,0,0,1]
	v_mad_i64_i32 v[158:159], s[40:41], v1, s12, v[158:159]
	v_cvt_scalef32_pk_fp4_f32 v171, v174, v175, v161 op_sel:[0,0,1,1]
	v_permlane16_swap_b32_e32 v168, v170
	s_nop 0
	v_permlane16_swap_b32_e32 v169, v171
	v_lshl_add_u64 v[156:157], v[158:159], 0, v[156:157]
	s_mov_b32 s78, s75
	s_mov_b64 s[40:41], s[4:5]
	s_mov_b64 s[42:43], s[38:39]
	s_mov_b64 vcc, s[0:1]
	global_store_dwordx4 v[156:157], v[168:171], off
	s_cbranch_vccnz .LBB5_17

.LBB5_17:
	s_waitcnt vmcnt(0)
	s_cmpk_gt_u32 s3, 0xff
	s_cbranch_scc1 .LBB5_19
.LBB5_19:
	s_barrier
